# INIT weight conversion stream: same prefetch repair (next item's loads stay in flight; gain hoisted; copies wait vmcnt(4))
# baseline (speedup 1.0000x reference)
; __device__ __forceinline__ void cvt_load(const CvtItem& it, float (&v)[32], int lane) {
; #pragma unroll
;     for (int i = 0; i < 32; ++i) { const int kk = 2 * i + (lane >> 5); v[i] = it.W[(size_t)(it.k0 + kk) * it.N + it.n0 + (lane & 31)]; }
; }
; template <int PH, bool PRB = false>
; __device__ __forceinline__ void run_phase(int layer, LAS unsigned char* lds, const int wv_) {
;     ...
;             if (gi < NITEMS) { CvtItem cur = item_of(gi); float v[32]; cvt_load(cur, v, lane);
.LBB0_104:
	s_ashr_i32 s41, s40, 31
	v_lshrrev_b32_e32 v67, 5, v1
	s_lshl_b64 s[8:9], s[40:41], 2
	v_add_u32_e32 v35, s30, v67
	v_and_b32_e32 v36, 31, v56
	s_add_u32 s6, s6, s8
	v_mov_b32_e32 v69, 0
	s_addc_u32 s7, s7, s9
	v_lshlrev_b32_e32 v68, 2, v36
	v_ashrrev_i32_e32 v2, 31, v35
	v_lshl_add_u64 v[26:27], s[6:7], 0, v[68:69]
	v_mul_lo_u32 v4, s4, v2
	v_mul_lo_u32 v5, s5, v35
	v_mad_u64_u32 v[2:3], s[6:7], s4, v35, 0
	v_add3_u32 v3, v3, v4, v5
	v_add_u32_e32 v4, 2, v35
	v_ashrrev_i32_e32 v5, 31, v4
	v_mul_lo_u32 v6, s4, v5
	v_mul_lo_u32 v7, s5, v4
	v_mad_u64_u32 v[4:5], s[6:7], s4, v4, 0
	v_add3_u32 v5, v5, v6, v7
	v_add_u32_e32 v6, 4, v35
	v_ashrrev_i32_e32 v7, 31, v6
	v_mul_lo_u32 v8, s4, v7
	v_mul_lo_u32 v9, s5, v6
	v_mad_u64_u32 v[6:7], s[6:7], s4, v6, 0
	v_add3_u32 v7, v7, v8, v9
	v_add_u32_e32 v8, 6, v35
	v_ashrrev_i32_e32 v9, 31, v8
	v_mul_lo_u32 v10, s4, v9
	v_mul_lo_u32 v11, s5, v8
	v_mad_u64_u32 v[8:9], s[6:7], s4, v8, 0
	v_add3_u32 v9, v9, v10, v11
	v_add_u32_e32 v10, 8, v35
	v_ashrrev_i32_e32 v11, 31, v10
	v_mul_lo_u32 v12, s4, v11
	v_mul_lo_u32 v13, s5, v10
	v_mad_u64_u32 v[10:11], s[6:7], s4, v10, 0
	v_add3_u32 v11, v11, v12, v13
	v_add_u32_e32 v12, 10, v35
	v_ashrrev_i32_e32 v13, 31, v12
	v_mul_lo_u32 v14, s4, v13
	v_mul_lo_u32 v15, s5, v12
	v_mad_u64_u32 v[12:13], s[6:7], s4, v12, 0
	v_add3_u32 v13, v13, v14, v15
	v_add_u32_e32 v14, 12, v35
	v_ashrrev_i32_e32 v15, 31, v14
	v_mul_lo_u32 v16, s4, v15
	v_mul_lo_u32 v17, s5, v14
	v_mad_u64_u32 v[14:15], s[6:7], s4, v14, 0
	v_add3_u32 v15, v15, v16, v17
	v_add_u32_e32 v16, 14, v35
	v_ashrrev_i32_e32 v17, 31, v16
	v_mul_lo_u32 v18, s4, v17
	v_mul_lo_u32 v19, s5, v16
	v_mad_u64_u32 v[16:17], s[6:7], s4, v16, 0
	v_lshl_add_u64 v[2:3], v[2:3], 2, v[26:27]
	v_lshl_add_u64 v[4:5], v[4:5], 2, v[26:27]
	v_lshl_add_u64 v[6:7], v[6:7], 2, v[26:27]
	v_lshl_add_u64 v[8:9], v[8:9], 2, v[26:27]
	v_lshl_add_u64 v[10:11], v[10:11], 2, v[26:27]
	v_add3_u32 v17, v17, v18, v19
	v_lshl_add_u64 v[12:13], v[12:13], 2, v[26:27]
	v_lshl_add_u64 v[14:15], v[14:15], 2, v[26:27]
	v_lshl_add_u64 v[16:17], v[16:17], 2, v[26:27]
	global_load_dword v2, v[2:3], off
	s_nop 0
	global_load_dword v3, v[4:5], off
	s_nop 0
	global_load_dword v4, v[6:7], off
	global_load_dword v5, v[8:9], off
	s_nop 0
	global_load_dword v6, v[10:11], off
	global_load_dword v7, v[12:13], off
	global_load_dword v8, v[14:15], off
	global_load_dword v9, v[16:17], off
	v_add_u32_e32 v10, 16, v35
	v_ashrrev_i32_e32 v11, 31, v10
	v_mul_lo_u32 v12, s4, v11
	v_mul_lo_u32 v13, s5, v10
	v_mad_u64_u32 v[10:11], s[6:7], s4, v10, 0
	v_add3_u32 v11, v11, v12, v13
	v_add_u32_e32 v12, 18, v35
	v_ashrrev_i32_e32 v13, 31, v12
	v_mul_lo_u32 v14, s4, v13
	v_mul_lo_u32 v15, s5, v12
	v_mad_u64_u32 v[12:13], s[6:7], s4, v12, 0
	v_add3_u32 v13, v13, v14, v15
	v_add_u32_e32 v14, 20, v35
	v_ashrrev_i32_e32 v15, 31, v14
	v_mul_lo_u32 v16, s4, v15
	v_mul_lo_u32 v17, s5, v14
	v_mad_u64_u32 v[14:15], s[6:7], s4, v14, 0
	v_add3_u32 v15, v15, v16, v17
	v_add_u32_e32 v16, 22, v35
	v_ashrrev_i32_e32 v17, 31, v16
	v_mul_lo_u32 v18, s4, v17
	v_mul_lo_u32 v19, s5, v16
	v_mad_u64_u32 v[16:17], s[6:7], s4, v16, 0
	v_add3_u32 v17, v17, v18, v19
	v_add_u32_e32 v18, 24, v35
	v_ashrrev_i32_e32 v19, 31, v18
	v_mul_lo_u32 v20, s4, v19
	v_mul_lo_u32 v21, s5, v18
	v_mad_u64_u32 v[18:19], s[6:7], s4, v18, 0
	v_add3_u32 v19, v19, v20, v21
	v_add_u32_e32 v20, 26, v35
	v_ashrrev_i32_e32 v21, 31, v20
	v_mul_lo_u32 v22, s4, v21
	v_mul_lo_u32 v23, s5, v20
	v_mad_u64_u32 v[20:21], s[6:7], s4, v20, 0
	v_add3_u32 v21, v21, v22, v23
	v_add_u32_e32 v22, 28, v35
	v_ashrrev_i32_e32 v23, 31, v22
	v_mul_lo_u32 v24, s4, v23
	v_mul_lo_u32 v25, s5, v22
	v_mad_u64_u32 v[22:23], s[6:7], s4, v22, 0
	v_add3_u32 v23, v23, v24, v25
	v_add_u32_e32 v24, 30, v35
	v_ashrrev_i32_e32 v25, 31, v24
	v_mul_lo_u32 v28, s4, v25
	v_mul_lo_u32 v29, s5, v24
	v_mad_u64_u32 v[24:25], s[6:7], s4, v24, 0
	v_add3_u32 v25, v25, v28, v29
	v_lshl_add_u64 v[10:11], v[10:11], 2, v[26:27]
	v_lshl_add_u64 v[12:13], v[12:13], 2, v[26:27]
	v_lshl_add_u64 v[14:15], v[14:15], 2, v[26:27]
	v_lshl_add_u64 v[16:17], v[16:17], 2, v[26:27]
	v_lshl_add_u64 v[18:19], v[18:19], 2, v[26:27]
	v_lshl_add_u64 v[20:21], v[20:21], 2, v[26:27]
	v_lshl_add_u64 v[22:23], v[22:23], 2, v[26:27]
	v_lshl_add_u64 v[24:25], v[24:25], 2, v[26:27]
	global_load_dword v10, v[10:11], off
	s_nop 0
	global_load_dword v11, v[12:13], off
	s_nop 0
	global_load_dword v12, v[14:15], off
	global_load_dword v13, v[16:17], off
	s_nop 0
	global_load_dword v14, v[18:19], off
	global_load_dword v15, v[20:21], off
	global_load_dword v16, v[22:23], off
	global_load_dword v17, v[24:25], off
	v_add_u32_e32 v18, 32, v35
	v_ashrrev_i32_e32 v19, 31, v18
	v_mul_lo_u32 v20, s4, v19
	v_mul_lo_u32 v21, s5, v18
	v_mad_u64_u32 v[18:19], s[6:7], s4, v18, 0
	v_add3_u32 v19, v19, v20, v21
	v_add_u32_e32 v20, 34, v35
	v_ashrrev_i32_e32 v21, 31, v20
	v_mul_lo_u32 v22, s4, v21
	v_mul_lo_u32 v23, s5, v20
	v_mad_u64_u32 v[20:21], s[6:7], s4, v20, 0
	v_add3_u32 v21, v21, v22, v23
; __device__ __forceinline__ void cvt_load(const CvtItem& it, float (&v)[32], int lane) {
; #pragma unroll
;     for (int i = 0; i < 32; ++i) { const int kk = 2 * i + (lane >> 5); v[i] = it.W[(size_t)(it.k0 + kk) * it.N + it.n0 + (lane & 31)]; }
; }
; template <int PH, bool PRB = false>
; __device__ __forceinline__ void run_phase(int layer, LAS unsigned char* lds, const int wv_) {
;     ...
;             if (gi < NITEMS) { CvtItem cur = item_of(gi); float v[32]; cvt_load(cur, v, lane);
	v_add_u32_e32 v22, 36, v35
	v_ashrrev_i32_e32 v23, 31, v22
	v_mul_lo_u32 v24, s4, v23
	v_mul_lo_u32 v25, s5, v22
	v_mad_u64_u32 v[22:23], s[6:7], s4, v22, 0
	v_add3_u32 v23, v23, v24, v25
	v_add_u32_e32 v24, 38, v35
	v_ashrrev_i32_e32 v25, 31, v24
	v_mul_lo_u32 v28, s4, v25
	v_mul_lo_u32 v29, s5, v24
	v_mad_u64_u32 v[24:25], s[6:7], s4, v24, 0
	v_add3_u32 v25, v25, v28, v29
	v_add_u32_e32 v28, 40, v35
	v_ashrrev_i32_e32 v29, 31, v28
	v_mul_lo_u32 v30, s4, v29
	v_mul_lo_u32 v31, s5, v28
	v_mad_u64_u32 v[28:29], s[6:7], s4, v28, 0
	v_add3_u32 v29, v29, v30, v31
	v_add_u32_e32 v30, 42, v35
	v_ashrrev_i32_e32 v31, 31, v30
	v_mul_lo_u32 v32, s4, v31
	v_mul_lo_u32 v33, s5, v30
	v_mad_u64_u32 v[30:31], s[6:7], s4, v30, 0
	v_add3_u32 v31, v31, v32, v33
	v_add_u32_e32 v32, 44, v35
	v_ashrrev_i32_e32 v33, 31, v32
	v_mul_lo_u32 v37, s4, v33
	v_mul_lo_u32 v38, s5, v32
	v_mad_u64_u32 v[32:33], s[6:7], s4, v32, 0
	v_add3_u32 v33, v33, v37, v38
	v_add_u32_e32 v37, 46, v35
	v_ashrrev_i32_e32 v38, 31, v37
	v_mul_lo_u32 v40, s4, v38
	v_mul_lo_u32 v41, s5, v37
	v_mad_u64_u32 v[38:39], s[6:7], s4, v37, 0
	v_add3_u32 v39, v39, v40, v41
	v_lshl_add_u64 v[18:19], v[18:19], 2, v[26:27]
	v_lshl_add_u64 v[20:21], v[20:21], 2, v[26:27]
	v_lshl_add_u64 v[22:23], v[22:23], 2, v[26:27]
	v_lshl_add_u64 v[24:25], v[24:25], 2, v[26:27]
	v_lshl_add_u64 v[28:29], v[28:29], 2, v[26:27]
	v_lshl_add_u64 v[30:31], v[30:31], 2, v[26:27]
	v_lshl_add_u64 v[32:33], v[32:33], 2, v[26:27]
	v_lshl_add_u64 v[38:39], v[38:39], 2, v[26:27]
	global_load_dword v18, v[18:19], off
	s_nop 0
	global_load_dword v19, v[20:21], off
	s_nop 0
	global_load_dword v20, v[22:23], off
	global_load_dword v21, v[24:25], off
	s_nop 0
	global_load_dword v22, v[28:29], off
	global_load_dword v23, v[30:31], off
	global_load_dword v24, v[32:33], off
	global_load_dword v25, v[38:39], off
	v_add_u32_e32 v28, 48, v35
	v_ashrrev_i32_e32 v29, 31, v28
	v_mul_lo_u32 v30, s4, v29
	v_mul_lo_u32 v31, s5, v28
	v_mad_u64_u32 v[28:29], s[6:7], s4, v28, 0
	v_add3_u32 v29, v29, v30, v31
	v_add_u32_e32 v30, 50, v35
	v_ashrrev_i32_e32 v31, 31, v30
	v_mul_lo_u32 v32, s4, v31
	v_mul_lo_u32 v33, s5, v30
	v_mad_u64_u32 v[30:31], s[6:7], s4, v30, 0
	v_add3_u32 v31, v31, v32, v33
	v_add_u32_e32 v32, 52, v35
	v_ashrrev_i32_e32 v33, 31, v32
	v_mul_lo_u32 v37, s4, v33
	v_mul_lo_u32 v38, s5, v32
	v_mad_u64_u32 v[32:33], s[6:7], s4, v32, 0
	v_add3_u32 v33, v33, v37, v38
	v_add_u32_e32 v37, 54, v35
	v_ashrrev_i32_e32 v38, 31, v37
	v_mul_lo_u32 v40, s4, v38
	v_mul_lo_u32 v41, s5, v37
	v_mad_u64_u32 v[38:39], s[6:7], s4, v37, 0
	v_add_u32_e32 v37, 56, v35
	v_add3_u32 v39, v39, v40, v41
	v_ashrrev_i32_e32 v40, 31, v37
	v_mul_lo_u32 v42, s4, v40
	v_mul_lo_u32 v43, s5, v37
	v_mad_u64_u32 v[40:41], s[6:7], s4, v37, 0
	v_add_u32_e32 v37, 58, v35
	v_add3_u32 v41, v41, v42, v43
	v_ashrrev_i32_e32 v42, 31, v37
	v_mul_lo_u32 v44, s4, v42
	v_mul_lo_u32 v45, s5, v37
	v_mad_u64_u32 v[42:43], s[6:7], s4, v37, 0
	v_add_u32_e32 v37, 60, v35
	v_add3_u32 v43, v43, v44, v45
	v_ashrrev_i32_e32 v44, 31, v37
	v_add_u32_e32 v35, 62, v35
	v_mul_lo_u32 v46, s4, v44
	v_mul_lo_u32 v47, s5, v37
	v_mad_u64_u32 v[44:45], s[6:7], s4, v37, 0
	v_ashrrev_i32_e32 v37, 31, v35
	v_add3_u32 v45, v45, v46, v47
	v_mul_lo_u32 v37, s4, v37
	v_mul_lo_u32 v48, s5, v35
	v_mad_u64_u32 v[46:47], s[4:5], s4, v35, 0
	v_lshl_add_u64 v[28:29], v[28:29], 2, v[26:27]
	v_lshl_add_u64 v[30:31], v[30:31], 2, v[26:27]
	v_lshl_add_u64 v[32:33], v[32:33], 2, v[26:27]
	v_add3_u32 v47, v47, v37, v48
	v_lshl_add_u64 v[38:39], v[38:39], 2, v[26:27]
	v_lshl_add_u64 v[40:41], v[40:41], 2, v[26:27]
	v_lshl_add_u64 v[42:43], v[42:43], 2, v[26:27]
	v_lshl_add_u64 v[44:45], v[44:45], 2, v[26:27]
	v_lshl_add_u64 v[46:47], v[46:47], 2, v[26:27]
	global_load_dword v26, v[28:29], off
	global_load_dword v27, v[30:31], off
	s_nop 0
	global_load_dword v28, v[32:33], off
	global_load_dword v29, v[38:39], off
	global_load_dword v30, v[40:41], off
	global_load_dword v31, v[42:43], off
	s_nop 0
	global_load_dword v32, v[44:45], off
	global_load_dword v33, v[46:47], off
	s_add_u32 s41, s44, 0x1e000000
	s_addc_u32 s48, s45, 0
	s_add_u32 s49, s44, 0x1d800000
	s_addc_u32 s60, s45, 0
	s_add_u32 s61, s44, 0x1d400000
	s_addc_u32 s62, s45, 0
	s_add_u32 s63, s44, 0x1d000000
	s_addc_u32 s64, s45, 0
	s_add_u32 s65, s44, 0x100000
	s_addc_u32 s66, s45, 0
	s_add_u32 s67, s44, 0x1a800000
	v_readlane_b32 s6, v254, 9
	s_addc_u32 s68, s45, 0
	v_lshrrev_b32_e32 v74, 3, v1
	v_and_b32_e32 v70, 56, v34
	v_add_u32_e32 v35, s6, v68
	v_mul_u32_u24_e32 v37, 0x84, v67
	s_add_u32 s69, s44, 0x1300000
	v_mul_u32_u24_e32 v34, 0x84, v70
	v_lshlrev_b32_e32 v38, 2, v74
	s_addc_u32 s70, s45, 0
	v_cmp_gt_u32_e64 s[4:5], 32, v1
	v_add3_u32 v75, s6, v34, v38
	v_mov_b32_e32 v71, v69
	v_or_b32_e32 v76, 8, v74
	v_or_b32_e32 v77, 16, v74
	v_or_b32_e32 v78, 24, v74
	v_lshlrev_b32_e32 v68, 2, v36
	v_add_u32_e32 v79, v35, v37
	s_mov_b32 s71, 0xc3e00000
	v_mov_b32_e32 v80, 0x43e00000
	s_waitcnt vmcnt(0)
	s_branch .LBB0_106

; __device__ __forceinline__ void cvt_finish(const CvtItem& it, float (&v)[32], LAS float* scr, int lane) {
;     if (it.g) { const float gv = it.g[it.k0 + lane];
; template <int PH, bool PRB = false>
; __device__ __forceinline__ void run_phase(int layer, LAS unsigned char* lds, const int wv_) {
;     ...
;                 for (;;) { const int gn = gi + NGW; const bool more = gn < NITEMS; CvtItem nxt = item_of(more ? gn : gi); float vn[32];
;                     if (more) cvt_load(nxt, vn, lane);
.LBB0_106:
	s_cmp_eq_u64 s[42:43], 0
	s_cbranch_scc1 .Lci_nog
	v_add_u32_e32 v110, s30, v1
	v_ashrrev_i32_e32 v111, 31, v110
	v_lshl_add_u64 v[110:111], v[110:111], 2, s[42:43]
	global_load_dword v108, v[110:111], off

; __device__ __forceinline__ void cvt_finish(const CvtItem& it, float (&v)[32], LAS float* scr, int lane) {
;     if (it.g) { const float gv = it.g[it.k0 + lane];
; #pragma unroll
.LBB0_129:
	s_and_b64 vcc, exec, s[6:7]
	s_cbranch_vccz .Lci_w32
	s_waitcnt vmcnt(0)
	s_branch .Lci_wd

; __device__ __forceinline__ void cvt_finish(const CvtItem& it, float (&v)[32], LAS float* scr, int lane) {
;     if (it.g) { const float gv = it.g[it.k0 + lane];
; #pragma unroll
;         for (int i = 0; i < 32; ++i) { const float g0 = __builtin_bit_cast(float, __builtin_amdgcn_readlane(__builtin_bit_cast(int, gv), 2 * i)), g1 = __builtin_bit_cast(float, __builtin_amdgcn_readlane(__builtin_bit_cast(int, gv), 2 * i + 1)); v[i] *= (lane >> 5) ? g1 : g0; } }
.Lci_wd:
	v_mov_b32_e32 v72, v108
	s_nop 0
	v_readlane_b32 s8, v72, 0
	v_readlane_b32 s9, v72, 1
	v_readlane_b32 s31, v72, 2
	v_readlane_b32 s51, v72, 3
	v_mov_b32_e32 v73, s9
	v_mov_b32_e32 v81, s8
	s_waitcnt lgkmcnt(0)
	v_mov_b32_e32 v82, s51
	v_mov_b32_e32 v83, s31
	v_cndmask_b32_e64 v73, v73, v81, s[4:5]
	v_cndmask_b32_e64 v81, v82, v83, s[4:5]
	v_readlane_b32 s8, v72, 28
	v_readlane_b32 s9, v72, 29
	v_mul_f32_e32 v2, v2, v73
	v_mul_f32_e32 v3, v3, v81
	v_mov_b32_e32 v73, s9
	v_mov_b32_e32 v81, s8
	v_cndmask_b32_e64 v73, v73, v81, s[4:5]
	v_readlane_b32 s8, v72, 30
	v_readlane_b32 s9, v72, 31
	v_mul_f32_e32 v16, v16, v73
	v_mov_b32_e32 v81, s8
	v_mov_b32_e32 v73, s9
	v_cndmask_b32_e64 v73, v73, v81, s[4:5]
	v_readlane_b32 s8, v72, 32
	v_readlane_b32 s9, v72, 33
	v_mul_f32_e32 v17, v17, v73
	v_mov_b32_e32 v81, s8
	v_mov_b32_e32 v73, s9
	v_cndmask_b32_e64 v73, v73, v81, s[4:5]
	v_readlane_b32 s8, v72, 34
	v_readlane_b32 s9, v72, 35
	v_mul_f32_e32 v18, v18, v73
	v_mov_b32_e32 v81, s8
	v_mov_b32_e32 v73, s9
	v_cndmask_b32_e64 v73, v73, v81, s[4:5]
	v_readlane_b32 s8, v72, 36
	v_readlane_b32 s9, v72, 37
	v_mul_f32_e32 v19, v19, v73
	v_mov_b32_e32 v81, s8
	v_mov_b32_e32 v73, s9
	v_cndmask_b32_e64 v73, v73, v81, s[4:5]
	v_readlane_b32 s8, v72, 38
	v_readlane_b32 s9, v72, 39
	v_mul_f32_e32 v20, v20, v73
	v_mov_b32_e32 v81, s8
	v_mov_b32_e32 v73, s9
	v_cndmask_b32_e64 v73, v73, v81, s[4:5]
	v_readlane_b32 s8, v72, 40
	v_readlane_b32 s9, v72, 41
	v_mul_f32_e32 v21, v21, v73
	v_mov_b32_e32 v81, s8
	v_mov_b32_e32 v73, s9
	v_cndmask_b32_e64 v73, v73, v81, s[4:5]
	v_readlane_b32 s8, v72, 42
	v_readlane_b32 s9, v72, 43
	v_mul_f32_e32 v22, v22, v73
	v_mov_b32_e32 v81, s8
	v_mov_b32_e32 v73, s9
	v_cndmask_b32_e64 v73, v73, v81, s[4:5]
	v_readlane_b32 s8, v72, 44
	v_readlane_b32 s9, v72, 45
	v_mul_f32_e32 v23, v23, v73
	v_mov_b32_e32 v81, s8
	v_mov_b32_e32 v73, s9
	v_cndmask_b32_e64 v73, v73, v81, s[4:5]
	v_readlane_b32 s8, v72, 46
	v_readlane_b32 s9, v72, 47
	v_mul_f32_e32 v24, v24, v73
	v_mov_b32_e32 v81, s8
	v_mov_b32_e32 v73, s9
	v_cndmask_b32_e64 v73, v73, v81, s[4:5]
	v_readlane_b32 s8, v72, 48
	v_readlane_b32 s9, v72, 49
	v_mul_f32_e32 v25, v25, v73
	v_mov_b32_e32 v81, s8
	v_mov_b32_e32 v73, s9
	v_cndmask_b32_e64 v73, v73, v81, s[4:5]
	v_readlane_b32 s8, v72, 50
	v_readlane_b32 s9, v72, 51
	v_mul_f32_e32 v26, v26, v73
	v_mov_b32_e32 v81, s8
	v_mov_b32_e32 v73, s9
	v_cndmask_b32_e64 v73, v73, v81, s[4:5]
	v_readlane_b32 s8, v72, 52
	v_readlane_b32 s9, v72, 53
	v_mul_f32_e32 v27, v27, v73
	v_mov_b32_e32 v81, s8
	v_mov_b32_e32 v73, s9
	v_cndmask_b32_e64 v73, v73, v81, s[4:5]
	v_readlane_b32 s8, v72, 54
	v_readlane_b32 s9, v72, 55
	v_mul_f32_e32 v28, v28, v73
	v_mov_b32_e32 v81, s8
	v_mov_b32_e32 v73, s9
	v_cndmask_b32_e64 v73, v73, v81, s[4:5]
	v_readlane_b32 s8, v72, 56
	v_readlane_b32 s9, v72, 57
	v_mul_f32_e32 v29, v29, v73
	v_mov_b32_e32 v81, s8
	v_mov_b32_e32 v73, s9
	v_cndmask_b32_e64 v73, v73, v81, s[4:5]
	v_readlane_b32 s8, v72, 58
	v_readlane_b32 s9, v72, 59
	v_mul_f32_e32 v30, v30, v73
	v_mov_b32_e32 v81, s8
	v_mov_b32_e32 v73, s9
	v_cndmask_b32_e64 v73, v73, v81, s[4:5]
	v_readlane_b32 s8, v72, 60
	v_readlane_b32 s9, v72, 61
	v_mul_f32_e32 v31, v31, v73
	v_mov_b32_e32 v81, s8
	v_mov_b32_e32 v73, s9
	v_readlane_b32 s54, v72, 4
	v_readlane_b32 s55, v72, 5
	v_readlane_b32 s56, v72, 6
	v_readlane_b32 s57, v72, 7
	v_readlane_b32 s59, v72, 8
	v_readlane_b32 s74, v72, 9
	v_readlane_b32 s75, v72, 10
	v_readlane_b32 s76, v72, 11
	v_readlane_b32 s77, v72, 12
	v_readlane_b32 s78, v72, 13
	v_readlane_b32 s79, v72, 14
	v_readlane_b32 s80, v72, 15
	v_readlane_b32 s81, v72, 16
	v_readlane_b32 s82, v72, 17
	v_readlane_b32 s83, v72, 18
	v_readlane_b32 s84, v72, 19
	v_readlane_b32 s85, v72, 20
	v_readlane_b32 s86, v72, 21
	v_readlane_b32 s87, v72, 22
	v_readlane_b32 s88, v72, 23
	v_readlane_b32 s89, v72, 24
	v_readlane_b32 s90, v72, 25
	v_readlane_b32 s91, v72, 26
	v_readlane_b32 s92, v72, 27
	v_cndmask_b32_e64 v73, v73, v81, s[4:5]
	v_readlane_b32 s8, v72, 62
	v_readlane_b32 s9, v72, 63
	v_mov_b32_e32 v84, s55
	v_mov_b32_e32 v85, s54
	v_mov_b32_e32 v86, s57
	v_mov_b32_e32 v87, s56
	v_mov_b32_e32 v88, s74
	v_mov_b32_e32 v89, s59
	v_mov_b32_e32 v90, s76
	v_mov_b32_e32 v91, s75
	v_mov_b32_e32 v92, s78
	v_mov_b32_e32 v93, s77
	v_mov_b32_e32 v94, s80
	v_mov_b32_e32 v95, s79
	v_mov_b32_e32 v96, s82
	v_mov_b32_e32 v97, s81
	v_mov_b32_e32 v98, s84
	v_mov_b32_e32 v99, s83
	v_mov_b32_e32 v100, s86
	v_mov_b32_e32 v101, s85
	v_mov_b32_e32 v102, s88
	v_mov_b32_e32 v103, s87
	v_mov_b32_e32 v104, s90
	v_mov_b32_e32 v105, s89
	v_mov_b32_e32 v106, s92
	v_mov_b32_e32 v107, s91
	v_mul_f32_e32 v32, v32, v73
	v_mov_b32_e32 v72, s9
	v_mov_b32_e32 v73, s8
	v_cndmask_b32_e64 v82, v84, v85, s[4:5]
	v_cndmask_b32_e64 v83, v86, v87, s[4:5]
	v_cndmask_b32_e64 v84, v88, v89, s[4:5]
	v_cndmask_b32_e64 v85, v90, v91, s[4:5]
	v_cndmask_b32_e64 v86, v92, v93, s[4:5]
	v_cndmask_b32_e64 v87, v94, v95, s[4:5]
	v_cndmask_b32_e64 v88, v96, v97, s[4:5]
	v_cndmask_b32_e64 v89, v98, v99, s[4:5]
	v_cndmask_b32_e64 v90, v100, v101, s[4:5]
	v_cndmask_b32_e64 v91, v102, v103, s[4:5]
	v_cndmask_b32_e64 v92, v104, v105, s[4:5]
	v_cndmask_b32_e64 v93, v106, v107, s[4:5]
	v_cndmask_b32_e64 v72, v72, v73, s[4:5]
	v_mul_f32_e32 v4, v4, v82
	v_mul_f32_e32 v5, v5, v83
	v_mul_f32_e32 v6, v6, v84
	v_mul_f32_e32 v7, v7, v85
	v_mul_f32_e32 v8, v8, v86
	v_mul_f32_e32 v9, v9, v87
	v_mul_f32_e32 v10, v10, v88
	v_mul_f32_e32 v11, v11, v89
	v_mul_f32_e32 v12, v12, v90
	v_mul_f32_e32 v13, v13, v91
	v_mul_f32_e32 v14, v14, v92
	v_mul_f32_e32 v15, v15, v93
	v_mul_f32_e32 v33, v33, v72
; #define LAS __attribute__((address_space(3)))
; #define CVT_PK_FP8_SAT(a, b, old, hi) __builtin_amdgcn_cvt_pk_fp8_f32(__builtin_amdgcn_fmed3f((a), -448.0f, 448.0f), __builtin_amdgcn_fmed3f((b), -448.0f, 448.0f), (old), (hi))
; __device__ __forceinline__ void cvt_finish(const CvtItem& it, float (&v)[32], LAS float* scr, int lane) {
;     ...
; #pragma unroll
;     for (int i = 0; i < 32; ++i) { const int kk = 2 * i + (lane >> 5); scr[kk * 33 + (lane & 31)] = v[i]; }
;     asm volatile("s_waitcnt lgkmcnt(0)" ::: "memory");
;     const int c = lane & 7;
; #pragma unroll
;     for (int j = 0; j < 4; ++j) { const int n = it.n0 + (lane >> 3) + 8 * j; const LAS float* s = scr + (8 * c) * 33 + (lane >> 3) + 8 * j;
;         const int row = it.rowmode == 0 ? n : ((n >> 7) * 256 + (it.rowmode == 2 ? 128 : 0) + (n & 127));
;         if (it.fp8) { int w0 = CVT_PK_FP8_SAT(s[0 * 33] * FP8_WSCALE, s[1 * 33] * FP8_WSCALE, 0, false); w0 = CVT_PK_FP8_SAT(s[2 * 33] * FP8_WSCALE, s[3 * 33] * FP8_WSCALE, w0, true);
;             int w1 = CVT_PK_FP8_SAT(s[4 * 33] * FP8_WSCALE, s[5 * 33] * FP8_WSCALE, 0, false); w1 = CVT_PK_FP8_SAT(s[6 * 33] * FP8_WSCALE, s[7 * 33] * FP8_WSCALE, w1, true);
;             u32x2 o8; o8.x = (unsigned)w0; o8.y = (unsigned)w1; *(u32x2*)((unsigned char*)it.WT + (size_t)row * it.K + it.k0 + 8 * c) = o8; continue; }
.LBB0_130:
	v_add_u32_e32 v72, 0x400, v79
	ds_write2_b32 v79, v2, v3 offset1:66
	ds_write2_b32 v79, v4, v5 offset0:132 offset1:198
	ds_write2_b32 v72, v6, v7 offset0:8 offset1:74
	ds_write2_b32 v72, v8, v9 offset0:140 offset1:206
	v_add_u32_e32 v72, 0x800, v79
	ds_write2_b32 v72, v10, v11 offset0:16 offset1:82
	ds_write2_b32 v72, v12, v13 offset0:148 offset1:214
	v_add_u32_e32 v72, 0xc00, v79
	ds_write2_b32 v72, v14, v15 offset0:24 offset1:90
	ds_write2_b32 v72, v16, v17 offset0:156 offset1:222
	v_add_u32_e32 v72, 0x1000, v79
	ds_write2_b32 v72, v18, v19 offset0:32 offset1:98
	ds_write2_b32 v72, v20, v21 offset0:164 offset1:230
	v_add_u32_e32 v72, 0x1400, v79
	ds_write2_b32 v72, v22, v23 offset0:40 offset1:106
	ds_write2_b32 v72, v24, v25 offset0:172 offset1:238
	v_add_u32_e32 v72, 0x1800, v79
	ds_write2_b32 v72, v26, v27 offset0:48 offset1:114
	ds_write2_b32 v72, v28, v29 offset0:180 offset1:246
	v_add_u32_e32 v72, 0x1c00, v79
	ds_write2_b32 v72, v30, v31 offset0:56 offset1:122
	ds_write2_b32 v72, v32, v33 offset0:188 offset1:254
	s_waitcnt lgkmcnt(0)
	ds_read_b32 v82, v75
	v_add_u32_e32 v73, s40, v74
	s_cmp_lg_u32 s38, 0
	s_cselect_b64 s[54:55], -1, 0
	s_cmp_eq_u32 s38, 0
	v_ashrrev_i32_e32 v81, 31, v73
	s_cbranch_scc1 .LBB0_134
	ds_read2_b32 v[84:85], v75 offset0:33 offset1:66
	s_waitcnt lgkmcnt(1)
	v_mul_f32_e32 v72, 0x42800000, v82
	ds_read2_b32 v[88:89], v75 offset0:99 offset1:132
	v_mov_b32_e32 v86, v69
	v_med3_f32 v72, v72, s71, v80
	s_waitcnt lgkmcnt(1)
	v_mul_f32_e32 v83, 0x42800000, v84
	v_med3_f32 v83, v83, s71, v80
	v_cvt_pk_fp8_f32 v86, v72, v83
	v_mul_f32_e32 v72, 0x42800000, v85
	ds_read2_b32 v[84:85], v75 offset0:165 offset1:198
	s_waitcnt lgkmcnt(1)
	v_mul_f32_e32 v83, 0x42800000, v88
	v_med3_f32 v72, v72, s71, v80
	v_med3_f32 v83, v83, s71, v80
	v_cvt_pk_fp8_f32 v86, v72, v83 op_sel:[0,0,1]
	s_waitcnt lgkmcnt(0)
	v_mul_f32_e32 v83, 0x42800000, v84
	ds_read_b32 v84, v75 offset:924
	v_mul_f32_e32 v72, 0x42800000, v89
	v_med3_f32 v72, v72, s71, v80
	v_med3_f32 v83, v83, s71, v80
	v_mov_b32_e32 v87, v69
	v_cvt_pk_fp8_f32 v87, v72, v83
	v_mul_f32_e32 v72, 0x42800000, v85
	s_waitcnt lgkmcnt(0)
	v_mul_f32_e32 v83, 0x42800000, v84
	v_mov_b64_e32 v[84:85], s[0:1]
	v_med3_f32 v72, v72, s71, v80
	v_med3_f32 v83, v83, s71, v80
	v_mad_u64_u32 v[84:85], s[8:9], v73, s39, v[84:85]
	v_cvt_pk_fp8_f32 v87, v72, v83 op_sel:[0,0,1]
	v_mov_b32_e32 v72, v85
	v_mad_u64_u32 v[88:89], s[8:9], v81, s39, v[72:73]
	v_mov_b32_e32 v85, v88
	s_ashr_i32 s31, s30, 31
	v_lshl_add_u64 v[84:85], v[84:85], 0, s[30:31]
	v_lshl_add_u64 v[84:85], v[84:85], 0, v[70:71]
	s_mov_b64 s[8:9], 0
	global_store_dwordx2 v[84:85], v[86:87], off
	s_branch .LBB0_135

; template <int PH, bool PRB = false>
; __device__ __forceinline__ void run_phase(int layer, LAS unsigned char* lds, const int wv_) {
;     ...
;                     cvt_finish(cur, v, scr, lane);
;                     if (!more) break;
; #pragma unroll
;                     for (int i = 0; i < 32; ++i) v[i] = vn[i];
;                     cur = nxt; gi = gn; } }
.LBB0_146:
	s_waitcnt lgkmcnt(0)
	s_and_b64 vcc, exec, s[6:7]
	s_cbranch_vccnz .LBB0_105
	s_waitcnt vmcnt(4)
	v_mov_b64_e32 v[2:3], v[34:35]
	s_mov_b32 s39, s58
	s_mov_b64 s[42:43], s[52:53]
	s_mov_b64 s[0:1], s[46:47]
	s_mov_b32 s30, s73
	s_mov_b32 s40, s50
	s_mov_b32 s38, s10
	v_mov_b64_e32 v[4:5], v[36:37]
	v_mov_b64_e32 v[6:7], v[38:39]
	v_mov_b64_e32 v[8:9], v[40:41]
	v_mov_b64_e32 v[10:11], v[42:43]
	v_mov_b64_e32 v[12:13], v[44:45]
	v_mov_b64_e32 v[14:15], v[46:47]
	v_mov_b64_e32 v[16:17], v[48:49]
	v_mov_b64_e32 v[18:19], v[50:51]
	v_mov_b64_e32 v[20:21], v[52:53]
	v_mov_b64_e32 v[22:23], v[54:55]
	v_mov_b64_e32 v[24:25], v[56:57]
	v_mov_b64_e32 v[26:27], v[58:59]
	v_mov_b64_e32 v[28:29], v[60:61]
	v_mov_b64_e32 v[30:31], v[62:63]
	v_mov_b64_e32 v[32:33], v[64:65]
	s_mov_b32 s24, s72
	s_branch .LBB0_105
